# plus: final-phase next-token routing record scalarised at the end of the iteration; retention-output epilogue rg loads all issued ahead of the first rn store
# speedup vs baseline: 1.0144x; 1.0001x over previous
.LBB0_399:
	ds_read_b128 v[86:89], v83
	ds_read_b128 v[90:93], v83 offset:64
	ds_read_b128 v[94:97], v83 offset:4608
	ds_read_b128 v[98:101], v83 offset:128
	ds_read_b128 v[102:105], v83 offset:4672
	v_add_u32_e32 v85, s0, v137
	s_waitcnt lgkmcnt(2)
	v_mfma_f32_16x16x32_bf16 v[94:97], v[94:97], v[74:77], 0
	ds_read_b128 v[106:109], v83 offset:192
	ds_read_b128 v[110:113], v83 offset:4736
	ds_read_b128 v[178:181], v83 offset:4800
	v_cmp_ge_u32_e32 vcc, v146, v82
	v_mfma_f32_16x16x32_bf16 v[86:89], v[86:89], v[74:77], 0
	v_mfma_f32_16x16x32_bf16 v[86:89], v[90:93], v[66:69], v[86:89]
	v_cvt_f32_i32_e32 v90, v85
	v_add_u32_e32 v91, -1, v85
	v_cvt_f32_i32_e32 v91, v91
	s_waitcnt lgkmcnt(4)
	v_mfma_f32_16x16x32_bf16 v[86:89], v[98:101], v[70:73], v[86:89]
	v_mul_f32_e32 v90, v149, v90
	v_mul_f32_e32 v90, 0x3fb8aa3b, v90
	v_mul_f32_e32 v91, v149, v91
	v_exp_f32_e32 v98, v90
	v_mul_f32_e32 v99, 0x3fb8aa3b, v91
	s_waitcnt lgkmcnt(3)
	v_mfma_f32_16x16x32_bf16 v[90:93], v[102:105], v[66:69], v[94:97]
	v_exp_f32_e32 v99, v99
	s_nop 1
	v_add_u32_e32 v94, -2, v85
	v_cvt_f32_i32_e32 v94, v94
	v_add_u32_e32 v97, -3, v85
	s_waitcnt lgkmcnt(2)
	v_mfma_f32_16x16x32_bf16 v[86:89], v[106:109], v[78:81], v[86:89]
	v_add_u32_e32 v95, 2, v82
	v_mul_f32_e32 v94, v149, v94
	v_mul_f32_e32 v94, 0x3fb8aa3b, v94
	v_exp_f32_e32 v96, v94
	v_cndmask_b32_e32 v94, 0, v98, vcc
	v_cvt_f32_i32_e32 v98, v97
	v_cmp_ge_u32_e32 vcc, v1, v95
	s_nop 0
	v_mov_b32_e32 v97, v88
	v_add_u32_e32 v88, 3, v82
	v_cndmask_b32_e32 v95, 0, v96, vcc
	v_mov_b32_e32 v96, v86
	v_mul_f32_e32 v86, v149, v98
	v_mul_f32_e32 v86, 0x3fb8aa3b, v86
	v_exp_f32_e32 v86, v86
	v_cmp_le_u32_e32 vcc, v88, v124
	v_pk_mul_f32 v[94:95], v[94:95], v[96:97]
	v_mov_b32_e32 v88, v87
	v_cndmask_b32_e32 v97, 0, v86, vcc
	v_cmp_gt_u32_e32 vcc, v146, v82
	v_add_u32_e32 v86, -16, v85
	v_cvt_f32_i32_e32 v98, v86
	v_cndmask_b32_e32 v96, 0, v99, vcc
	v_pk_mul_f32 v[86:87], v[96:97], v[88:89]
	v_subrev_u32_e32 v96, 18, v85
	v_cvt_f32_i32_e32 v96, v96
	v_subrev_u32_e32 v89, 17, v85
	v_subrev_u32_e32 v85, 19, v85
	s_waitcnt lgkmcnt(1)
	v_mfma_f32_16x16x32_bf16 v[90:93], v[110:113], v[70:73], v[90:93]
	v_cvt_f32_i32_e32 v89, v89
	v_cvt_f32_i32_e32 v85, v85
	v_mul_f32_e32 v96, v149, v96
	v_mul_f32_e32 v88, v149, v98
	v_mul_f32_e32 v96, 0x3fb8aa3b, v96
	s_waitcnt lgkmcnt(0)
	v_mfma_f32_16x16x32_bf16 v[90:93], v[178:181], v[78:81], v[90:93]
	v_mul_f32_e32 v88, 0x3fb8aa3b, v88
	v_mul_f32_e32 v89, v149, v89
	v_exp_f32_e32 v96, v96
	v_mul_f32_e32 v85, v149, v85
	v_exp_f32_e32 v88, v88
	v_mul_f32_e32 v89, 0x3fb8aa3b, v89
	v_mul_f32_e32 v85, 0x3fb8aa3b, v85
	v_exp_f32_e32 v98, v89
	v_add_u32_e32 v89, 18, v82
	v_exp_f32_e32 v85, v85
	v_add_u32_e32 v99, 16, v82
	v_cmp_ge_u32_e32 vcc, v1, v89
	v_mov_b32_e32 v97, v92
	v_mov_b32_e32 v92, v91
	v_cndmask_b32_e32 v89, 0, v96, vcc
	v_cmp_ge_u32_e32 vcc, v146, v99
	v_mov_b32_e32 v96, v90
	v_add_u32_e32 v90, 19, v82
	v_cndmask_b32_e32 v88, 0, v88, vcc
	v_cmp_le_u32_e32 vcc, v90, v124
	v_pk_mul_f32 v[88:89], v[88:89], v[96:97]
	s_nop 0
	v_cndmask_b32_e32 v97, 0, v85, vcc
	v_cmp_gt_u32_e32 vcc, v146, v99
	s_nop 1
	v_cndmask_b32_e32 v96, 0, v98, vcc
	v_pk_mul_f32 v[90:91], v[96:97], v[92:93]
	v_bfe_u32 v93, v87, 16, 1
	v_bfe_u32 v85, v91, 16, 1
	v_bfe_u32 v92, v90, 16, 1
	v_add3_u32 v87, v87, v93, s63
	v_add3_u32 v85, v91, v85, s63
	v_bfe_u32 v91, v94, 16, 1
	v_bfe_u32 v93, v88, 16, 1
	v_bfe_u32 v96, v86, 16, 1
	v_add3_u32 v90, v90, v92, s63
	v_bfe_u32 v92, v95, 16, 1
	v_add3_u32 v88, v88, v93, s63
	v_add3_u32 v91, v94, v91, s63
	v_add3_u32 v86, v86, v96, s63
	v_add3_u32 v92, v95, v92, s63
	v_lshrrev_b32_e32 v91, 16, v91
	v_lshrrev_b32_e32 v88, 16, v88
	v_lshrrev_b32_e32 v92, 16, v92
	v_and_or_b32 v88, v90, s64, v88
	v_and_or_b32 v86, v86, s64, v91
	ds_read_b64_tr_b16 v[90:91], v84 offset:0
	v_and_or_b32 v87, v87, s64, v92
	ds_read_b64_tr_b16 v[92:93], v84 offset:8704
	v_bfe_u32 v96, v89, 16, 1
	ds_read_b64_tr_b16 v[94:95], v84 offset:32
	v_add3_u32 v89, v89, v96, s63
	ds_read_b64_tr_b16 v[96:97], v84 offset:8736
	ds_read_b64_tr_b16 v[98:99], v84 offset:64
	ds_read_b64_tr_b16 v[100:101], v84 offset:8768
	ds_read_b64_tr_b16 v[102:103], v84 offset:96
	ds_read_b64_tr_b16 v[104:105], v84 offset:8800
	ds_read_b64_tr_b16 v[106:107], v84 offset:128
	ds_read_b64_tr_b16 v[108:109], v84 offset:8832
	ds_read_b64_tr_b16 v[110:111], v84 offset:160
	ds_read_b64_tr_b16 v[112:113], v84 offset:8864
	ds_read_b64_tr_b16 v[178:179], v84 offset:192
	ds_read_b64_tr_b16 v[180:181], v84 offset:8896
	ds_read_b64_tr_b16 v[182:183], v84 offset:224
	ds_read_b64_tr_b16 v[184:185], v84 offset:8928
	s_waitcnt lgkmcnt(0)
	v_lshrrev_b32_e32 v89, 16, v89
	v_and_or_b32 v89, v85, s64, v89
	s_nop 1
	v_mfma_f32_16x16x32_bf16 v[62:65], v[90:93], v[86:89], v[62:65]
	ds_read_b64_tr_b16 v[90:91], v84 offset:256
	ds_read_b64_tr_b16 v[92:93], v84 offset:8960
	v_mfma_f32_16x16x32_bf16 v[58:61], v[94:97], v[86:89], v[58:61]
	ds_read_b64_tr_b16 v[94:95], v84 offset:288
	ds_read_b64_tr_b16 v[96:97], v84 offset:8992
	v_mfma_f32_16x16x32_bf16 v[54:57], v[98:101], v[86:89], v[54:57]
	ds_read_b64_tr_b16 v[98:99], v84 offset:320
	ds_read_b64_tr_b16 v[100:101], v84 offset:9024
	v_mfma_f32_16x16x32_bf16 v[50:53], v[102:105], v[86:89], v[50:53]
	ds_read_b64_tr_b16 v[102:103], v84 offset:352
	ds_read_b64_tr_b16 v[104:105], v84 offset:9056
	v_mfma_f32_16x16x32_bf16 v[46:49], v[106:109], v[86:89], v[46:49]
	ds_read_b64_tr_b16 v[106:107], v84 offset:384
	ds_read_b64_tr_b16 v[108:109], v84 offset:9088
	v_mfma_f32_16x16x32_bf16 v[42:45], v[110:113], v[86:89], v[42:45]
	ds_read_b64_tr_b16 v[110:111], v84 offset:416
	ds_read_b64_tr_b16 v[112:113], v84 offset:9120
	ds_read_b64_tr_b16 v[186:187], v84 offset:448
	ds_read_b64_tr_b16 v[188:189], v84 offset:9152
	v_mfma_f32_16x16x32_bf16 v[38:41], v[178:181], v[86:89], v[38:41]
	ds_read_b64_tr_b16 v[178:179], v84 offset:480
	ds_read_b64_tr_b16 v[180:181], v84 offset:9184
	s_waitcnt lgkmcnt(0)
	v_mfma_f32_16x16x32_bf16 v[34:37], v[182:185], v[86:89], v[34:37]
	v_mfma_f32_16x16x32_bf16 v[30:33], v[90:93], v[86:89], v[30:33]
	s_sub_i32 s0, s0, 32
	s_add_i32 s1, s3, s0
	v_add_u32_e32 v84, 0x4400, v84
	v_mfma_f32_16x16x32_bf16 v[26:29], v[94:97], v[86:89], v[26:29]
	v_add_u32_e32 v83, 0x2400, v83
	v_add_u32_e32 v82, 32, v82
	s_cmp_lg_u32 s1, 0
	v_mfma_f32_16x16x32_bf16 v[22:25], v[98:101], v[86:89], v[22:25]
	v_mfma_f32_16x16x32_bf16 v[18:21], v[102:105], v[86:89], v[18:21]
	v_mfma_f32_16x16x32_bf16 v[14:17], v[106:109], v[86:89], v[14:17]
	v_mfma_f32_16x16x32_bf16 v[10:13], v[110:113], v[86:89], v[10:13]
	v_mfma_f32_16x16x32_bf16 v[6:9], v[186:189], v[86:89], v[6:9]
	v_mfma_f32_16x16x32_bf16 v[2:5], v[178:181], v[86:89], v[2:5]
	s_cbranch_scc1 .LBB0_399
	v_pk_mul_f32 v[66:67], v[64:65], v[64:65]
	v_pk_mul_f32 v[68:69], v[62:63], v[62:63]
	v_mov_b32_e32 v153, v115
	v_pk_mov_b32 v[70:71], v[68:69], v[66:67] op_sel:[1,0]
	v_mov_b32_e32 v69, v67
	v_pk_add_f32 v[66:67], v[70:71], v[68:69]
	v_pk_mul_f32 v[68:69], v[60:61], v[60:61]
	v_pk_mul_f32 v[70:71], v[58:59], v[58:59]
	v_pk_add_f32 v[66:67], v[66:67], v[66:67] op_sel:[0,1] op_sel_hi:[1,0]
	v_pk_mov_b32 v[72:73], v[70:71], v[68:69] op_sel:[1,0]
	v_mov_b32_e32 v71, v69
	v_pk_add_f32 v[68:69], v[72:73], v[70:71]
	v_mul_f32_e32 v70, v50, v50
	v_mul_f32_e32 v71, v51, v51
	v_pk_add_f32 v[68:69], v[68:69], v[68:69] op_sel:[0,1] op_sel_hi:[1,0]
	v_mov_b32_e32 v67, v70
	v_mov_b32_e32 v69, v71
	v_pk_add_f32 v[66:67], v[66:67], v[68:69]
	v_mul_f32_e32 v68, v55, v55
	v_mul_f32_e32 v70, v57, v57
	v_mul_f32_e32 v72, v52, v52
	v_mul_f32_e32 v73, v53, v53
	v_pk_fma_f32 v[68:69], v[54:55], v[54:55], v[68:69] op_sel_hi:[1,1,0]
	v_pk_fma_f32 v[70:71], v[56:57], v[56:57], v[70:71] op_sel_hi:[1,1,0]
	v_mov_b32_e32 v69, v72
	v_mov_b32_e32 v71, v73
	v_pk_add_f32 v[68:69], v[68:69], v[70:71]
	v_pk_mul_f32 v[70:71], v[46:47], v[46:47]
	v_pk_add_f32 v[66:67], v[66:67], v[68:69]
	v_pk_mul_f32 v[68:69], v[48:49], v[48:49]
	v_pk_add_f32 v[66:67], v[66:67], v[66:67] op_sel:[0,1] op_sel_hi:[1,0]
	v_pk_mov_b32 v[72:73], v[70:71], v[68:69] op_sel:[1,0]
	v_mov_b32_e32 v71, v69
	v_pk_add_f32 v[68:69], v[72:73], v[70:71]
	v_mul_f32_e32 v70, v38, v38
	v_mul_f32_e32 v71, v39, v39
	v_pk_add_f32 v[68:69], v[68:69], v[68:69] op_sel:[0,1] op_sel_hi:[1,0]
	v_mov_b32_e32 v67, v70
	v_mov_b32_e32 v69, v71
	v_pk_add_f32 v[66:67], v[66:67], v[68:69]
	v_mul_f32_e32 v68, v43, v43
	v_mul_f32_e32 v70, v45, v45
	v_mul_f32_e32 v72, v40, v40
	v_mul_f32_e32 v73, v41, v41
	v_pk_fma_f32 v[68:69], v[42:43], v[42:43], v[68:69] op_sel_hi:[1,1,0]
	v_pk_fma_f32 v[70:71], v[44:45], v[44:45], v[70:71] op_sel_hi:[1,1,0]
	v_mov_b32_e32 v69, v72
	v_mov_b32_e32 v71, v73
	v_pk_add_f32 v[68:69], v[68:69], v[70:71]
	v_pk_mul_f32 v[70:71], v[34:35], v[34:35]
	v_pk_add_f32 v[66:67], v[66:67], v[68:69]
	v_pk_mul_f32 v[68:69], v[36:37], v[36:37]
	v_pk_add_f32 v[66:67], v[66:67], v[66:67] op_sel:[0,1] op_sel_hi:[1,0]
	v_pk_mov_b32 v[72:73], v[70:71], v[68:69] op_sel:[1,0]
	v_mov_b32_e32 v71, v69
	v_pk_add_f32 v[68:69], v[72:73], v[70:71]
	v_mul_f32_e32 v70, v26, v26
	v_mul_f32_e32 v71, v27, v27
	v_pk_add_f32 v[68:69], v[68:69], v[68:69] op_sel:[0,1] op_sel_hi:[1,0]
	v_mov_b32_e32 v67, v70
	v_mov_b32_e32 v69, v71
	v_pk_add_f32 v[66:67], v[66:67], v[68:69]
	v_mul_f32_e32 v68, v31, v31
	v_mul_f32_e32 v70, v33, v33
	v_mul_f32_e32 v72, v28, v28
	v_mul_f32_e32 v73, v29, v29
	v_pk_fma_f32 v[68:69], v[30:31], v[30:31], v[68:69] op_sel_hi:[1,1,0]
	v_pk_fma_f32 v[70:71], v[32:33], v[32:33], v[70:71] op_sel_hi:[1,1,0]
	v_mov_b32_e32 v69, v72
	v_mov_b32_e32 v71, v73
	v_pk_add_f32 v[68:69], v[68:69], v[70:71]
	v_pk_mul_f32 v[70:71], v[22:23], v[22:23]
	v_pk_add_f32 v[66:67], v[66:67], v[68:69]
	v_pk_mul_f32 v[68:69], v[24:25], v[24:25]
	v_mul_f32_e32 v74, v14, v14
	v_pk_mov_b32 v[72:73], v[70:71], v[68:69] op_sel:[1,0]
	v_mov_b32_e32 v71, v69
	v_pk_add_f32 v[68:69], v[72:73], v[70:71]
	v_lshl_add_u64 v[70:71], v[156:157], 0, s[42:43]
	v_lshl_add_u64 v[72:73], v[70:71], 0, v[152:153]
	v_add_co_u32_e32 v70, vcc, s67, v72
	v_mul_f32_e32 v75, v15, v15
	s_nop 0
	v_addc_co_u32_e32 v71, vcc, 0, v73, vcc
	global_load_dwordx2 v[70:71], v[70:71], off offset:2048
	v_pk_add_f32 v[66:67], v[66:67], v[66:67] op_sel:[0,1] op_sel_hi:[1,0]
	v_pk_add_f32 v[68:69], v[68:69], v[68:69] op_sel:[0,1] op_sel_hi:[1,0]
	v_mov_b32_e32 v67, v74
	v_mov_b32_e32 v69, v75
	v_pk_add_f32 v[66:67], v[66:67], v[68:69]
	v_mul_f32_e32 v68, v19, v19
	v_mul_f32_e32 v74, v21, v21
	v_mul_f32_e32 v76, v16, v16
	v_mul_f32_e32 v77, v17, v17
	v_pk_fma_f32 v[68:69], v[18:19], v[18:19], v[68:69] op_sel_hi:[1,1,0]
	v_pk_fma_f32 v[74:75], v[20:21], v[20:21], v[74:75] op_sel_hi:[1,1,0]
	v_mov_b32_e32 v69, v76
	v_mov_b32_e32 v75, v77
	v_pk_add_f32 v[68:69], v[68:69], v[74:75]
	v_pk_mul_f32 v[74:75], v[10:11], v[10:11]
	v_pk_add_f32 v[66:67], v[66:67], v[68:69]
	v_pk_mul_f32 v[68:69], v[12:13], v[12:13]
	v_pk_add_f32 v[66:67], v[66:67], v[66:67] op_sel:[0,1] op_sel_hi:[1,0]
	v_pk_mov_b32 v[76:77], v[74:75], v[68:69] op_sel:[1,0]
	v_mov_b32_e32 v75, v69
	v_pk_add_f32 v[68:69], v[76:77], v[74:75]
	v_mul_f32_e32 v74, v2, v2
	v_mul_f32_e32 v75, v3, v3
	v_pk_add_f32 v[68:69], v[68:69], v[68:69] op_sel:[0,1] op_sel_hi:[1,0]
	v_mov_b32_e32 v67, v74
	v_mov_b32_e32 v69, v75
	v_pk_add_f32 v[66:67], v[66:67], v[68:69]
	v_mul_f32_e32 v68, v7, v7
	v_mul_f32_e32 v74, v9, v9
	v_mul_f32_e32 v76, v4, v4
	v_mul_f32_e32 v77, v5, v5
	v_pk_fma_f32 v[68:69], v[6:7], v[6:7], v[68:69] op_sel_hi:[1,1,0]
	v_pk_fma_f32 v[74:75], v[8:9], v[8:9], v[74:75] op_sel_hi:[1,1,0]
	v_mov_b32_e32 v69, v76
	v_mov_b32_e32 v75, v77
	v_pk_add_f32 v[68:69], v[68:69], v[74:75]
	v_mov_b32_e32 v92, v62
	v_pk_add_f32 v[66:67], v[66:67], v[68:69]
	v_and_b32_e32 v68, 64, v176
	v_add_u32_e32 v74, 64, v68
	v_lshl_add_u64 v[68:69], v[72:73], 0, s[22:23]
	global_load_dwordx2 v[72:73], v[68:69], off offset:32
	v_add_f32_e32 v66, v66, v67
	v_xor_b32_e32 v67, 16, v176
	v_cmp_lt_i32_e32 vcc, v67, v74
	global_load_dwordx2 v[76:77], v[68:69], off offset:416
	global_load_dwordx2 v[78:79], v[68:69], off offset:448
	global_load_dwordx2 v[80:81], v[68:69], off offset:480
	v_cndmask_b32_e32 v67, v176, v67, vcc
	v_lshlrev_b32_e32 v67, 2, v67
	ds_bpermute_b32 v67, v67, v66
	global_load_dwordx2 v[88:89], v[68:69], off offset:64
	v_mov_b32_e32 v93, v64
	v_mov_b32_e32 v64, v63
	s_add_i32 s40, s40, s33
	s_waitcnt lgkmcnt(0)
	v_add_f32_e32 v66, v66, v67
	v_xor_b32_e32 v67, 32, v176
	v_cmp_lt_i32_e32 vcc, v67, v74
	v_mov_b64_e32 v[74:75], s[10:11]
	v_mad_u64_u32 v[74:75], s[0:1], v154, s66, v[74:75]
	v_cndmask_b32_e32 v67, v176, v67, vcc
	v_lshlrev_b32_e32 v67, 2, v67
	ds_bpermute_b32 v67, v67, v66
	v_mad_i32_i24 v75, v155, s66, v75
	v_lshl_add_u64 v[74:75], v[74:75], 0, s[42:43]
	v_lshl_add_u64 v[84:85], v[74:75], 0, v[152:153]
	v_lshl_add_u64 v[74:75], v[84:85], 0, s[38:39]
	s_waitcnt lgkmcnt(0)
	v_add_f32_e32 v66, v66, v67
	v_fmamk_f32 v66, v66, 0x3b800000, v167
	v_mul_f32_e32 v67, 0x4b800000, v66
	v_cmp_gt_f32_e32 vcc, s65, v66
	s_cmpk_lt_i32 s40, 0x200
	s_waitcnt vmcnt(5)
	v_lshlrev_b32_e32 v82, 16, v70
	v_cndmask_b32_e32 v66, v66, v67, vcc
	v_rsq_f32_e32 v66, v66
	v_lshlrev_b32_e32 v83, 16, v71
	v_mul_f32_e32 v87, 0xbfb8aa3b, v83
	v_exp_f32_e32 v87, v87
	v_mul_f32_e32 v67, 0x45800000, v66
	v_cndmask_b32_e32 v66, v66, v67, vcc
	v_mul_f32_e32 v67, 0xbfb8aa3b, v82
	v_exp_f32_e32 v67, v67
	v_and_b32_e32 v70, 0xffff0000, v70
	v_and_b32_e32 v71, 0xffff0000, v71
	v_add_f32_e32 v62, 1.0, v87
	v_add_f32_e32 v67, 1.0, v67
	v_rcp_f32_e32 v86, v67
	v_mul_f32_e32 v67, 0xbfb8aa3b, v70
	v_rcp_f32_e32 v87, v62
	v_mul_f32_e32 v62, 0xbfb8aa3b, v71
	v_exp_f32_e32 v67, v67
	v_exp_f32_e32 v62, v62
	v_pk_mul_f32 v[82:83], v[86:87], v[82:83]
	v_add_co_u32_e32 v84, vcc, s68, v84
	v_add_f32_e32 v67, 1.0, v67
	v_add_f32_e32 v62, 1.0, v62
	v_rcp_f32_e32 v90, v67
	v_rcp_f32_e32 v91, v62
	v_pk_mul_f32 v[62:63], v[64:65], v[66:67] op_sel_hi:[1,0]
	v_pk_mul_f32 v[92:93], v[92:93], v[66:67] op_sel_hi:[1,0]
	v_addc_co_u32_e32 v85, vcc, 0, v85, vcc
	v_pk_mul_f32 v[64:65], v[90:91], v[70:71]
	v_pk_mul_f32 v[82:83], v[82:83], v[92:93]
	v_pk_mul_f32 v[62:63], v[64:65], v[62:63]
	v_and_b32_sdwa v64, v83, v177 dst_sel:DWORD dst_unused:UNUSED_PAD src0_sel:WORD_1 src1_sel:DWORD
	v_and_b32_sdwa v67, v63, v177 dst_sel:DWORD dst_unused:UNUSED_PAD src0_sel:WORD_1 src1_sel:DWORD
	v_and_b32_sdwa v70, v62, v177 dst_sel:DWORD dst_unused:UNUSED_PAD src0_sel:WORD_1 src1_sel:DWORD
	v_and_b32_sdwa v65, v82, v177 dst_sel:DWORD dst_unused:UNUSED_PAD src0_sel:WORD_1 src1_sel:DWORD
	v_add3_u32 v63, v63, v67, s63
	v_add3_u32 v62, v62, v70, s63
	v_add3_u32 v65, v82, v65, s63
	v_add3_u32 v64, v83, v64, s63
	v_and_b32_e32 v63, 0xffff0000, v63
	v_and_b32_e32 v62, 0xffff0000, v62
	v_or_b32_sdwa v63, v63, v64 dst_sel:DWORD dst_unused:UNUSED_PAD src0_sel:DWORD src1_sel:WORD_1
	v_or_b32_sdwa v62, v62, v65 dst_sel:DWORD dst_unused:UNUSED_PAD src0_sel:DWORD src1_sel:WORD_1
	global_load_dwordx2 v[64:65], v[68:69], off offset:96
	global_load_dwordx2 v[70:71], v[68:69], off offset:128
	global_load_dwordx2 v[230:231], v[68:69], off offset:160
	global_load_dwordx2 v[232:233], v[68:69], off offset:192
	global_load_dwordx2 v[234:235], v[68:69], off offset:224
	global_load_dwordx2 v[236:237], v[68:69], off offset:256
	global_load_dwordx2 v[238:239], v[68:69], off offset:288
	global_load_dwordx2 v[240:241], v[68:69], off offset:320
	global_load_dwordx2 v[242:243], v[68:69], off offset:352
	global_load_dwordx2 v[244:245], v[68:69], off offset:384
	s_waitcnt vmcnt(6)
	v_lshlrev_b32_e32 v82, 16, v72
	v_mul_f32_e32 v67, 0xbfb8aa3b, v82
	v_exp_f32_e32 v67, v67
	v_lshlrev_b32_e32 v83, 16, v73
	v_and_b32_e32 v72, 0xffff0000, v72
	global_store_dwordx2 v[84:85], v[62:63], off offset:2048
	v_add_f32_e32 v62, 1.0, v67
	v_mul_f32_e32 v63, 0xbfb8aa3b, v72
	v_mul_f32_e32 v67, 0xbfb8aa3b, v83
	v_exp_f32_e32 v63, v63
	v_exp_f32_e32 v67, v67
	v_and_b32_e32 v73, 0xffff0000, v73
	v_mov_b32_e32 v86, v58
	v_add_f32_e32 v63, 1.0, v63
	v_add_f32_e32 v58, 1.0, v67
	v_rcp_f32_e32 v84, v63
	v_rcp_f32_e32 v63, v58
	v_mul_f32_e32 v58, 0xbfb8aa3b, v73
	v_exp_f32_e32 v58, v58
	v_rcp_f32_e32 v62, v62
	v_mov_b32_e32 v87, v60
	v_pk_mul_f32 v[86:87], v[86:87], v[66:67] op_sel_hi:[1,0]
	v_add_f32_e32 v58, 1.0, v58
	v_rcp_f32_e32 v85, v58
	v_pk_mul_f32 v[62:63], v[62:63], v[82:83]
	v_mov_b32_e32 v60, v59
	v_pk_mul_f32 v[62:63], v[86:87], v[62:63]
	v_pk_mul_f32 v[58:59], v[60:61], v[66:67] op_sel_hi:[1,0]
	v_pk_mul_f32 v[60:61], v[84:85], v[72:73]
	v_mov_b32_e32 v82, v54
	v_pk_mul_f32 v[58:59], v[58:59], v[60:61]
	v_and_b32_sdwa v61, v62, v177 dst_sel:DWORD dst_unused:UNUSED_PAD src0_sel:WORD_1 src1_sel:DWORD
	v_add3_u32 v61, v62, v61, s63
	v_and_b32_sdwa v62, v59, v177 dst_sel:DWORD dst_unused:UNUSED_PAD src0_sel:WORD_1 src1_sel:DWORD
	v_and_b32_sdwa v60, v63, v177 dst_sel:DWORD dst_unused:UNUSED_PAD src0_sel:WORD_1 src1_sel:DWORD
	v_add3_u32 v59, v59, v62, s63
	v_add3_u32 v60, v63, v60, s63
	v_and_b32_e32 v59, 0xffff0000, v59
	v_or_b32_sdwa v59, v59, v60 dst_sel:DWORD dst_unused:UNUSED_PAD src0_sel:DWORD src1_sel:WORD_1
	s_waitcnt vmcnt(3)
	v_lshlrev_b32_e32 v60, 16, v88
	v_mul_f32_e32 v62, 0xbfb8aa3b, v60
	v_and_b32_sdwa v63, v58, v177 dst_sel:DWORD dst_unused:UNUSED_PAD src0_sel:WORD_1 src1_sel:DWORD
	v_exp_f32_e32 v62, v62
	v_add3_u32 v58, v58, v63, s63
	v_and_b32_e32 v58, 0xffff0000, v58
	v_or_b32_sdwa v58, v58, v61 dst_sel:DWORD dst_unused:UNUSED_PAD src0_sel:DWORD src1_sel:WORD_1
	global_store_dwordx2 v[74:75], v[58:59], off offset:32
	v_lshlrev_b32_e32 v61, 16, v89
	v_add_f32_e32 v58, 1.0, v62
	v_and_b32_e32 v62, 0xffff0000, v88
	v_mul_f32_e32 v59, 0xbfb8aa3b, v62
	v_mul_f32_e32 v67, 0xbfb8aa3b, v61
	v_exp_f32_e32 v59, v59
	v_exp_f32_e32 v67, v67
	v_and_b32_e32 v63, 0xffff0000, v89
	v_rcp_f32_e32 v58, v58
	v_add_f32_e32 v59, 1.0, v59
	v_add_f32_e32 v54, 1.0, v67
	v_rcp_f32_e32 v72, v59
	v_rcp_f32_e32 v59, v54
	v_mul_f32_e32 v54, 0xbfb8aa3b, v63
	v_exp_f32_e32 v54, v54
	v_mov_b32_e32 v83, v56
	v_pk_mul_f32 v[82:83], v[82:83], v[66:67] op_sel_hi:[1,0]
	v_pk_mul_f32 v[58:59], v[58:59], v[60:61]
	v_add_f32_e32 v54, 1.0, v54
	v_rcp_f32_e32 v73, v54
	v_mov_b32_e32 v56, v55
	v_pk_mul_f32 v[58:59], v[82:83], v[58:59]
	v_pk_mul_f32 v[54:55], v[56:57], v[66:67] op_sel_hi:[1,0]
	v_pk_mul_f32 v[56:57], v[72:73], v[62:63]
	s_waitcnt vmcnt(3)
	v_and_b32_e32 v60, 0xffff0000, v64
	v_pk_mul_f32 v[54:55], v[54:55], v[56:57]
	v_and_b32_sdwa v57, v58, v177 dst_sel:DWORD dst_unused:UNUSED_PAD src0_sel:WORD_1 src1_sel:DWORD
	v_add3_u32 v57, v58, v57, s63
	v_and_b32_sdwa v58, v55, v177 dst_sel:DWORD dst_unused:UNUSED_PAD src0_sel:WORD_1 src1_sel:DWORD
	v_and_b32_sdwa v56, v59, v177 dst_sel:DWORD dst_unused:UNUSED_PAD src0_sel:WORD_1 src1_sel:DWORD
	v_add3_u32 v55, v55, v58, s63
	v_add3_u32 v56, v59, v56, s63
	v_and_b32_e32 v55, 0xffff0000, v55
	v_or_b32_sdwa v55, v55, v56 dst_sel:DWORD dst_unused:UNUSED_PAD src0_sel:DWORD src1_sel:WORD_1
	v_lshlrev_b32_e32 v56, 16, v64
	v_mul_f32_e32 v58, 0xbfb8aa3b, v56
	v_and_b32_sdwa v59, v54, v177 dst_sel:DWORD dst_unused:UNUSED_PAD src0_sel:WORD_1 src1_sel:DWORD
	v_exp_f32_e32 v58, v58
	v_add3_u32 v54, v54, v59, s63
	v_and_b32_e32 v54, 0xffff0000, v54
	v_or_b32_sdwa v54, v54, v57 dst_sel:DWORD dst_unused:UNUSED_PAD src0_sel:DWORD src1_sel:WORD_1
	global_store_dwordx2 v[74:75], v[54:55], off offset:64
	v_add_f32_e32 v54, 1.0, v58
	v_lshlrev_b32_e32 v57, 16, v65
	v_mul_f32_e32 v55, 0xbfb8aa3b, v60
	v_mul_f32_e32 v62, 0xbfb8aa3b, v57
	v_exp_f32_e32 v55, v55
	v_exp_f32_e32 v63, v62
	v_and_b32_e32 v61, 0xffff0000, v65
	v_mov_b32_e32 v64, v50
	v_add_f32_e32 v55, 1.0, v55
	v_add_f32_e32 v50, 1.0, v63
	v_rcp_f32_e32 v62, v55
	v_rcp_f32_e32 v55, v50
	v_mul_f32_e32 v50, 0xbfb8aa3b, v61
	v_exp_f32_e32 v50, v50
	v_rcp_f32_e32 v54, v54
	v_mov_b32_e32 v65, v52
	v_pk_mul_f32 v[64:65], v[64:65], v[66:67] op_sel_hi:[1,0]
	v_add_f32_e32 v50, 1.0, v50
	v_rcp_f32_e32 v63, v50
	v_pk_mul_f32 v[54:55], v[54:55], v[56:57]
	v_mov_b32_e32 v52, v51
	v_pk_mul_f32 v[54:55], v[64:65], v[54:55]
	v_pk_mul_f32 v[50:51], v[52:53], v[66:67] op_sel_hi:[1,0]
	v_pk_mul_f32 v[52:53], v[62:63], v[60:61]
	s_waitcnt vmcnt(4)
	v_and_b32_e32 v56, 0xffff0000, v70
	v_pk_mul_f32 v[50:51], v[50:51], v[52:53]
	v_and_b32_sdwa v52, v55, v177 dst_sel:DWORD dst_unused:UNUSED_PAD src0_sel:WORD_1 src1_sel:DWORD
	v_and_b32_sdwa v53, v54, v177 dst_sel:DWORD dst_unused:UNUSED_PAD src0_sel:WORD_1 src1_sel:DWORD
	v_add3_u32 v53, v54, v53, s63
	v_add3_u32 v52, v55, v52, s63
	v_and_b32_sdwa v54, v51, v177 dst_sel:DWORD dst_unused:UNUSED_PAD src0_sel:WORD_1 src1_sel:DWORD
	v_and_b32_sdwa v55, v50, v177 dst_sel:DWORD dst_unused:UNUSED_PAD src0_sel:WORD_1 src1_sel:DWORD
	v_add3_u32 v51, v51, v54, s63
	v_add3_u32 v50, v50, v55, s63
	v_and_b32_e32 v51, 0xffff0000, v51
	v_and_b32_e32 v50, 0xffff0000, v50
	v_or_b32_sdwa v51, v51, v52 dst_sel:DWORD dst_unused:UNUSED_PAD src0_sel:DWORD src1_sel:WORD_1
	v_or_b32_sdwa v50, v50, v53 dst_sel:DWORD dst_unused:UNUSED_PAD src0_sel:DWORD src1_sel:WORD_1
	global_store_dwordx2 v[74:75], v[50:51], off offset:96
	v_lshlrev_b32_e32 v53, 16, v71
	v_mul_f32_e32 v55, 0xbfb8aa3b, v56
	v_mul_f32_e32 v60, 0xbfb8aa3b, v53
	v_exp_f32_e32 v55, v55
	v_exp_f32_e32 v61, v60
	v_lshlrev_b32_e32 v52, 16, v70
	v_mul_f32_e32 v54, 0xbfb8aa3b, v52
	v_and_b32_e32 v57, 0xffff0000, v71
	v_add_f32_e32 v55, 1.0, v55
	v_mov_b32_e32 v62, v46
	v_add_f32_e32 v46, 1.0, v61
	v_exp_f32_e32 v54, v54
	v_rcp_f32_e32 v60, v55
	v_rcp_f32_e32 v55, v46
	v_mul_f32_e32 v46, 0xbfb8aa3b, v57
	v_exp_f32_e32 v46, v46
	v_add_f32_e32 v54, 1.0, v54
	v_rcp_f32_e32 v54, v54
	v_mov_b32_e32 v63, v48
	v_add_f32_e32 v46, 1.0, v46
	v_rcp_f32_e32 v61, v46
	v_pk_mul_f32 v[62:63], v[62:63], v[66:67] op_sel_hi:[1,0]
	v_pk_mul_f32 v[52:53], v[54:55], v[52:53]
	v_mov_b32_e32 v48, v47
	v_pk_mul_f32 v[52:53], v[62:63], v[52:53]
	v_pk_mul_f32 v[46:47], v[48:49], v[66:67] op_sel_hi:[1,0]
	v_pk_mul_f32 v[48:49], v[60:61], v[56:57]
	v_mov_b32_e32 v60, v42
	v_pk_mul_f32 v[46:47], v[46:47], v[48:49]
	v_and_b32_sdwa v49, v52, v177 dst_sel:DWORD dst_unused:UNUSED_PAD src0_sel:WORD_1 src1_sel:DWORD
	v_add3_u32 v55, v52, v49, s63
	v_and_b32_sdwa v49, v47, v177 dst_sel:DWORD dst_unused:UNUSED_PAD src0_sel:WORD_1 src1_sel:DWORD
	v_and_b32_sdwa v48, v53, v177 dst_sel:DWORD dst_unused:UNUSED_PAD src0_sel:WORD_1 src1_sel:DWORD
	v_add3_u32 v47, v47, v49, s63
	v_add3_u32 v48, v53, v48, s63
	v_and_b32_sdwa v52, v46, v177 dst_sel:DWORD dst_unused:UNUSED_PAD src0_sel:WORD_1 src1_sel:DWORD
	v_and_b32_e32 v47, 0xffff0000, v47
	v_add3_u32 v46, v46, v52, s63
	v_or_b32_sdwa v47, v47, v48 dst_sel:DWORD dst_unused:UNUSED_PAD src0_sel:DWORD src1_sel:WORD_1
	s_waitcnt vmcnt(4)
	v_lshlrev_b32_e32 v54, 16, v230
	v_mul_f32_e32 v56, 0xbfb8aa3b, v54
	v_exp_f32_e32 v56, v56
	v_and_b32_e32 v46, 0xffff0000, v46
	v_or_b32_sdwa v46, v46, v55 dst_sel:DWORD dst_unused:UNUSED_PAD src0_sel:DWORD src1_sel:WORD_1
	global_store_dwordx2 v[74:75], v[46:47], off offset:128
	v_lshlrev_b32_e32 v55, 16, v231
	v_add_f32_e32 v46, 1.0, v56
	v_and_b32_e32 v56, 0xffff0000, v230
	v_mul_f32_e32 v47, 0xbfb8aa3b, v56
	v_mul_f32_e32 v58, 0xbfb8aa3b, v55
	v_exp_f32_e32 v47, v47
	v_and_b32_e32 v57, 0xffff0000, v231
	v_exp_f32_e32 v59, v58
	v_rcp_f32_e32 v46, v46
	v_add_f32_e32 v47, 1.0, v47
	v_rcp_f32_e32 v58, v47
	v_add_f32_e32 v42, 1.0, v59
	v_rcp_f32_e32 v47, v42
	v_mul_f32_e32 v42, 0xbfb8aa3b, v57
	v_exp_f32_e32 v42, v42
	v_mov_b32_e32 v61, v44
	v_pk_mul_f32 v[60:61], v[60:61], v[66:67] op_sel_hi:[1,0]
	v_pk_mul_f32 v[46:47], v[46:47], v[54:55]
	v_add_f32_e32 v42, 1.0, v42
	v_rcp_f32_e32 v59, v42
	v_mov_b32_e32 v44, v43
	v_pk_mul_f32 v[46:47], v[60:61], v[46:47]
	v_pk_mul_f32 v[42:43], v[44:45], v[66:67] op_sel_hi:[1,0]
	v_pk_mul_f32 v[44:45], v[58:59], v[56:57]
	v_mov_b32_e32 v54, v38
	v_pk_mul_f32 v[42:43], v[42:43], v[44:45]
	v_and_b32_sdwa v45, v46, v177 dst_sel:DWORD dst_unused:UNUSED_PAD src0_sel:WORD_1 src1_sel:DWORD
	v_add3_u32 v45, v46, v45, s63
	v_and_b32_sdwa v46, v43, v177 dst_sel:DWORD dst_unused:UNUSED_PAD src0_sel:WORD_1 src1_sel:DWORD
	v_and_b32_sdwa v44, v47, v177 dst_sel:DWORD dst_unused:UNUSED_PAD src0_sel:WORD_1 src1_sel:DWORD
	v_add3_u32 v43, v43, v46, s63
	v_add3_u32 v44, v47, v44, s63
	v_and_b32_e32 v43, 0xffff0000, v43
	v_or_b32_sdwa v43, v43, v44 dst_sel:DWORD dst_unused:UNUSED_PAD src0_sel:DWORD src1_sel:WORD_1
	s_waitcnt vmcnt(3)
	v_lshlrev_b32_e32 v44, 16, v232
	v_mul_f32_e32 v46, 0xbfb8aa3b, v44
	v_and_b32_sdwa v47, v42, v177 dst_sel:DWORD dst_unused:UNUSED_PAD src0_sel:WORD_1 src1_sel:DWORD
	v_exp_f32_e32 v46, v46
	v_add3_u32 v42, v42, v47, s63
	v_and_b32_e32 v42, 0xffff0000, v42
	v_or_b32_sdwa v42, v42, v45 dst_sel:DWORD dst_unused:UNUSED_PAD src0_sel:DWORD src1_sel:WORD_1
	global_store_dwordx2 v[74:75], v[42:43], off offset:160
	v_lshlrev_b32_e32 v45, 16, v233
	v_add_f32_e32 v42, 1.0, v46
	v_and_b32_e32 v46, 0xffff0000, v232
	v_mul_f32_e32 v43, 0xbfb8aa3b, v46
	v_mul_f32_e32 v50, 0xbfb8aa3b, v45
	v_exp_f32_e32 v43, v43
	v_and_b32_e32 v47, 0xffff0000, v233
	v_exp_f32_e32 v51, v50
	v_rcp_f32_e32 v42, v42
	v_add_f32_e32 v43, 1.0, v43
	v_rcp_f32_e32 v50, v43
	v_add_f32_e32 v38, 1.0, v51
	v_rcp_f32_e32 v43, v38
	v_mul_f32_e32 v38, 0xbfb8aa3b, v47
	v_exp_f32_e32 v38, v38
	v_mov_b32_e32 v55, v40
	v_pk_mul_f32 v[54:55], v[54:55], v[66:67] op_sel_hi:[1,0]
	v_pk_mul_f32 v[42:43], v[42:43], v[44:45]
	v_add_f32_e32 v38, 1.0, v38
	v_rcp_f32_e32 v51, v38
	v_mov_b32_e32 v40, v39
	v_pk_mul_f32 v[42:43], v[54:55], v[42:43]
	v_pk_mul_f32 v[38:39], v[40:41], v[66:67] op_sel_hi:[1,0]
	v_pk_mul_f32 v[40:41], v[50:51], v[46:47]
	s_waitcnt vmcnt(3)
	v_and_b32_e32 v44, 0xffff0000, v234
	v_pk_mul_f32 v[38:39], v[38:39], v[40:41]
	v_and_b32_sdwa v41, v42, v177 dst_sel:DWORD dst_unused:UNUSED_PAD src0_sel:WORD_1 src1_sel:DWORD
	v_add3_u32 v41, v42, v41, s63
	v_and_b32_sdwa v42, v39, v177 dst_sel:DWORD dst_unused:UNUSED_PAD src0_sel:WORD_1 src1_sel:DWORD
	v_and_b32_sdwa v40, v43, v177 dst_sel:DWORD dst_unused:UNUSED_PAD src0_sel:WORD_1 src1_sel:DWORD
	v_add3_u32 v39, v39, v42, s63
	v_add3_u32 v40, v43, v40, s63
	v_and_b32_e32 v39, 0xffff0000, v39
	v_or_b32_sdwa v39, v39, v40 dst_sel:DWORD dst_unused:UNUSED_PAD src0_sel:DWORD src1_sel:WORD_1
	v_lshlrev_b32_e32 v40, 16, v234
	v_mul_f32_e32 v42, 0xbfb8aa3b, v40
	v_and_b32_sdwa v43, v38, v177 dst_sel:DWORD dst_unused:UNUSED_PAD src0_sel:WORD_1 src1_sel:DWORD
	v_exp_f32_e32 v42, v42
	v_add3_u32 v38, v38, v43, s63
	v_and_b32_e32 v38, 0xffff0000, v38
	v_or_b32_sdwa v38, v38, v41 dst_sel:DWORD dst_unused:UNUSED_PAD src0_sel:DWORD src1_sel:WORD_1
	global_store_dwordx2 v[74:75], v[38:39], off offset:192
	v_add_f32_e32 v38, 1.0, v42
	v_lshlrev_b32_e32 v41, 16, v235
	v_mul_f32_e32 v39, 0xbfb8aa3b, v44
	v_mul_f32_e32 v46, 0xbfb8aa3b, v41
	v_exp_f32_e32 v39, v39
	v_exp_f32_e32 v47, v46
	v_and_b32_e32 v45, 0xffff0000, v235
	v_mov_b32_e32 v48, v34
	v_add_f32_e32 v39, 1.0, v39
	v_add_f32_e32 v34, 1.0, v47
	v_rcp_f32_e32 v46, v39
	v_rcp_f32_e32 v39, v34
	v_mul_f32_e32 v34, 0xbfb8aa3b, v45
	v_exp_f32_e32 v34, v34
	v_rcp_f32_e32 v38, v38
	v_mov_b32_e32 v49, v36
	v_pk_mul_f32 v[48:49], v[48:49], v[66:67] op_sel_hi:[1,0]
	v_add_f32_e32 v34, 1.0, v34
	v_rcp_f32_e32 v47, v34
	v_pk_mul_f32 v[38:39], v[38:39], v[40:41]
	v_mov_b32_e32 v36, v35
	v_pk_mul_f32 v[38:39], v[48:49], v[38:39]
	v_pk_mul_f32 v[34:35], v[36:37], v[66:67] op_sel_hi:[1,0]
	v_pk_mul_f32 v[36:37], v[46:47], v[44:45]
	s_waitcnt vmcnt(4)
	v_and_b32_e32 v40, 0xffff0000, v236
	v_pk_mul_f32 v[34:35], v[34:35], v[36:37]
	v_and_b32_sdwa v36, v39, v177 dst_sel:DWORD dst_unused:UNUSED_PAD src0_sel:WORD_1 src1_sel:DWORD
	v_and_b32_sdwa v37, v38, v177 dst_sel:DWORD dst_unused:UNUSED_PAD src0_sel:WORD_1 src1_sel:DWORD
	v_add3_u32 v37, v38, v37, s63
	v_add3_u32 v36, v39, v36, s63
	v_and_b32_sdwa v38, v35, v177 dst_sel:DWORD dst_unused:UNUSED_PAD src0_sel:WORD_1 src1_sel:DWORD
	v_and_b32_sdwa v39, v34, v177 dst_sel:DWORD dst_unused:UNUSED_PAD src0_sel:WORD_1 src1_sel:DWORD
	v_add3_u32 v35, v35, v38, s63
	v_add3_u32 v34, v34, v39, s63
	v_and_b32_e32 v35, 0xffff0000, v35
	v_and_b32_e32 v34, 0xffff0000, v34
	v_or_b32_sdwa v35, v35, v36 dst_sel:DWORD dst_unused:UNUSED_PAD src0_sel:DWORD src1_sel:WORD_1
	v_or_b32_sdwa v34, v34, v37 dst_sel:DWORD dst_unused:UNUSED_PAD src0_sel:DWORD src1_sel:WORD_1
	global_store_dwordx2 v[74:75], v[34:35], off offset:224
	v_lshlrev_b32_e32 v37, 16, v237
	v_mul_f32_e32 v39, 0xbfb8aa3b, v40
	v_mul_f32_e32 v44, 0xbfb8aa3b, v37
	v_exp_f32_e32 v39, v39
	v_exp_f32_e32 v45, v44
	v_lshlrev_b32_e32 v36, 16, v236
	v_mul_f32_e32 v38, 0xbfb8aa3b, v36
	v_and_b32_e32 v41, 0xffff0000, v237
	v_add_f32_e32 v39, 1.0, v39
	v_mov_b32_e32 v46, v30
	v_add_f32_e32 v30, 1.0, v45
	v_exp_f32_e32 v38, v38
	v_rcp_f32_e32 v44, v39
	v_rcp_f32_e32 v39, v30
	v_mul_f32_e32 v30, 0xbfb8aa3b, v41
	v_exp_f32_e32 v30, v30
	v_add_f32_e32 v38, 1.0, v38
	v_rcp_f32_e32 v38, v38
	v_mov_b32_e32 v47, v32
	v_add_f32_e32 v30, 1.0, v30
	v_rcp_f32_e32 v45, v30
	v_pk_mul_f32 v[46:47], v[46:47], v[66:67] op_sel_hi:[1,0]
	v_pk_mul_f32 v[36:37], v[38:39], v[36:37]
	v_mov_b32_e32 v32, v31
	v_pk_mul_f32 v[36:37], v[46:47], v[36:37]
	v_pk_mul_f32 v[30:31], v[32:33], v[66:67] op_sel_hi:[1,0]
	v_pk_mul_f32 v[32:33], v[44:45], v[40:41]
	v_mov_b32_e32 v44, v26
	v_pk_mul_f32 v[30:31], v[30:31], v[32:33]
	v_and_b32_sdwa v33, v36, v177 dst_sel:DWORD dst_unused:UNUSED_PAD src0_sel:WORD_1 src1_sel:DWORD
	v_add3_u32 v39, v36, v33, s63
	v_and_b32_sdwa v33, v31, v177 dst_sel:DWORD dst_unused:UNUSED_PAD src0_sel:WORD_1 src1_sel:DWORD
	v_and_b32_sdwa v32, v37, v177 dst_sel:DWORD dst_unused:UNUSED_PAD src0_sel:WORD_1 src1_sel:DWORD
	v_add3_u32 v31, v31, v33, s63
	v_add3_u32 v32, v37, v32, s63
	v_and_b32_sdwa v36, v30, v177 dst_sel:DWORD dst_unused:UNUSED_PAD src0_sel:WORD_1 src1_sel:DWORD
	v_and_b32_e32 v31, 0xffff0000, v31
	v_add3_u32 v30, v30, v36, s63
	v_or_b32_sdwa v31, v31, v32 dst_sel:DWORD dst_unused:UNUSED_PAD src0_sel:DWORD src1_sel:WORD_1
	s_waitcnt vmcnt(4)
	v_lshlrev_b32_e32 v38, 16, v238
	v_mul_f32_e32 v40, 0xbfb8aa3b, v38
	v_exp_f32_e32 v40, v40
	v_and_b32_e32 v30, 0xffff0000, v30
	v_or_b32_sdwa v30, v30, v39 dst_sel:DWORD dst_unused:UNUSED_PAD src0_sel:DWORD src1_sel:WORD_1
	global_store_dwordx2 v[74:75], v[30:31], off offset:256
	v_lshlrev_b32_e32 v39, 16, v239
	v_add_f32_e32 v30, 1.0, v40
	v_and_b32_e32 v40, 0xffff0000, v238
	v_mul_f32_e32 v31, 0xbfb8aa3b, v40
	v_mul_f32_e32 v42, 0xbfb8aa3b, v39
	v_exp_f32_e32 v31, v31
	v_and_b32_e32 v41, 0xffff0000, v239
	v_exp_f32_e32 v43, v42
	v_rcp_f32_e32 v30, v30
	v_add_f32_e32 v31, 1.0, v31
	v_rcp_f32_e32 v42, v31
	v_add_f32_e32 v26, 1.0, v43
	v_rcp_f32_e32 v31, v26
	v_mul_f32_e32 v26, 0xbfb8aa3b, v41
	v_exp_f32_e32 v26, v26
	v_mov_b32_e32 v45, v28
	v_pk_mul_f32 v[44:45], v[44:45], v[66:67] op_sel_hi:[1,0]
	v_pk_mul_f32 v[30:31], v[30:31], v[38:39]
	v_add_f32_e32 v26, 1.0, v26
	v_rcp_f32_e32 v43, v26
	v_mov_b32_e32 v28, v27
	v_pk_mul_f32 v[30:31], v[44:45], v[30:31]
	v_pk_mul_f32 v[26:27], v[28:29], v[66:67] op_sel_hi:[1,0]
	v_pk_mul_f32 v[28:29], v[42:43], v[40:41]
	v_mov_b32_e32 v38, v22
	v_pk_mul_f32 v[26:27], v[26:27], v[28:29]
	v_and_b32_sdwa v29, v30, v177 dst_sel:DWORD dst_unused:UNUSED_PAD src0_sel:WORD_1 src1_sel:DWORD
	v_add3_u32 v29, v30, v29, s63
	v_and_b32_sdwa v30, v27, v177 dst_sel:DWORD dst_unused:UNUSED_PAD src0_sel:WORD_1 src1_sel:DWORD
	v_and_b32_sdwa v28, v31, v177 dst_sel:DWORD dst_unused:UNUSED_PAD src0_sel:WORD_1 src1_sel:DWORD
	v_add3_u32 v27, v27, v30, s63
	v_add3_u32 v28, v31, v28, s63
	v_and_b32_e32 v27, 0xffff0000, v27
	v_or_b32_sdwa v27, v27, v28 dst_sel:DWORD dst_unused:UNUSED_PAD src0_sel:DWORD src1_sel:WORD_1
	s_waitcnt vmcnt(3)
	v_lshlrev_b32_e32 v28, 16, v240
	v_mul_f32_e32 v30, 0xbfb8aa3b, v28
	v_and_b32_sdwa v31, v26, v177 dst_sel:DWORD dst_unused:UNUSED_PAD src0_sel:WORD_1 src1_sel:DWORD
	v_exp_f32_e32 v30, v30
	v_add3_u32 v26, v26, v31, s63
	v_and_b32_e32 v26, 0xffff0000, v26
	v_or_b32_sdwa v26, v26, v29 dst_sel:DWORD dst_unused:UNUSED_PAD src0_sel:DWORD src1_sel:WORD_1
	global_store_dwordx2 v[74:75], v[26:27], off offset:288
	v_lshlrev_b32_e32 v29, 16, v241
	v_add_f32_e32 v26, 1.0, v30
	v_and_b32_e32 v30, 0xffff0000, v240
	v_mul_f32_e32 v27, 0xbfb8aa3b, v30
	v_mul_f32_e32 v34, 0xbfb8aa3b, v29
	v_exp_f32_e32 v27, v27
	v_and_b32_e32 v31, 0xffff0000, v241
	v_exp_f32_e32 v35, v34
	v_rcp_f32_e32 v26, v26
	v_add_f32_e32 v27, 1.0, v27
	v_rcp_f32_e32 v34, v27
	v_add_f32_e32 v22, 1.0, v35
	v_rcp_f32_e32 v27, v22
	v_mul_f32_e32 v22, 0xbfb8aa3b, v31
	v_exp_f32_e32 v22, v22
	v_mov_b32_e32 v39, v24
	v_pk_mul_f32 v[38:39], v[38:39], v[66:67] op_sel_hi:[1,0]
	v_pk_mul_f32 v[26:27], v[26:27], v[28:29]
	v_add_f32_e32 v22, 1.0, v22
	v_rcp_f32_e32 v35, v22
	v_mov_b32_e32 v24, v23
	v_pk_mul_f32 v[26:27], v[38:39], v[26:27]
	v_pk_mul_f32 v[22:23], v[24:25], v[66:67] op_sel_hi:[1,0]
	v_pk_mul_f32 v[24:25], v[34:35], v[30:31]
	v_mov_b32_e32 v30, v18
	v_pk_mul_f32 v[22:23], v[22:23], v[24:25]
	v_and_b32_sdwa v25, v26, v177 dst_sel:DWORD dst_unused:UNUSED_PAD src0_sel:WORD_1 src1_sel:DWORD
	v_add3_u32 v25, v26, v25, s63
	v_and_b32_sdwa v26, v23, v177 dst_sel:DWORD dst_unused:UNUSED_PAD src0_sel:WORD_1 src1_sel:DWORD
	v_and_b32_sdwa v24, v27, v177 dst_sel:DWORD dst_unused:UNUSED_PAD src0_sel:WORD_1 src1_sel:DWORD
	v_add3_u32 v23, v23, v26, s63
	v_add3_u32 v24, v27, v24, s63
	v_and_b32_e32 v23, 0xffff0000, v23
	v_or_b32_sdwa v23, v23, v24 dst_sel:DWORD dst_unused:UNUSED_PAD src0_sel:DWORD src1_sel:WORD_1
	s_waitcnt vmcnt(3)
	v_lshlrev_b32_e32 v24, 16, v242
	v_mul_f32_e32 v26, 0xbfb8aa3b, v24
	v_and_b32_sdwa v27, v22, v177 dst_sel:DWORD dst_unused:UNUSED_PAD src0_sel:WORD_1 src1_sel:DWORD
	v_exp_f32_e32 v26, v26
	v_add3_u32 v22, v22, v27, s63
	v_and_b32_e32 v22, 0xffff0000, v22
	v_or_b32_sdwa v22, v22, v25 dst_sel:DWORD dst_unused:UNUSED_PAD src0_sel:DWORD src1_sel:WORD_1
	global_store_dwordx2 v[74:75], v[22:23], off offset:320
	v_lshlrev_b32_e32 v25, 16, v243
	v_add_f32_e32 v22, 1.0, v26
	v_and_b32_e32 v26, 0xffff0000, v242
	v_mul_f32_e32 v23, 0xbfb8aa3b, v26
	v_mul_f32_e32 v28, 0xbfb8aa3b, v25
	v_exp_f32_e32 v23, v23
	v_exp_f32_e32 v29, v28
	v_and_b32_e32 v27, 0xffff0000, v243
	v_rcp_f32_e32 v22, v22
	v_add_f32_e32 v23, 1.0, v23
	v_add_f32_e32 v18, 1.0, v29
	v_rcp_f32_e32 v28, v23
	v_rcp_f32_e32 v23, v18
	v_mul_f32_e32 v18, 0xbfb8aa3b, v27
	v_exp_f32_e32 v18, v18
	v_mov_b32_e32 v31, v20
	v_pk_mul_f32 v[30:31], v[30:31], v[66:67] op_sel_hi:[1,0]
	v_pk_mul_f32 v[22:23], v[22:23], v[24:25]
	v_add_f32_e32 v18, 1.0, v18
	v_rcp_f32_e32 v29, v18
	v_mov_b32_e32 v20, v19
	v_pk_mul_f32 v[22:23], v[30:31], v[22:23]
	v_pk_mul_f32 v[18:19], v[20:21], v[66:67] op_sel_hi:[1,0]
	v_pk_mul_f32 v[20:21], v[28:29], v[26:27]
	v_mov_b32_e32 v26, v14
	v_pk_mul_f32 v[18:19], v[18:19], v[20:21]
	v_and_b32_sdwa v21, v22, v177 dst_sel:DWORD dst_unused:UNUSED_PAD src0_sel:WORD_1 src1_sel:DWORD
	v_add3_u32 v21, v22, v21, s63
	v_and_b32_sdwa v22, v19, v177 dst_sel:DWORD dst_unused:UNUSED_PAD src0_sel:WORD_1 src1_sel:DWORD
	v_and_b32_sdwa v20, v23, v177 dst_sel:DWORD dst_unused:UNUSED_PAD src0_sel:WORD_1 src1_sel:DWORD
	v_add3_u32 v19, v19, v22, s63
	v_add3_u32 v20, v23, v20, s63
	v_and_b32_e32 v19, 0xffff0000, v19
	v_or_b32_sdwa v19, v19, v20 dst_sel:DWORD dst_unused:UNUSED_PAD src0_sel:DWORD src1_sel:WORD_1
	s_waitcnt vmcnt(3)
	v_lshlrev_b32_e32 v20, 16, v244
	v_mul_f32_e32 v22, 0xbfb8aa3b, v20
	v_and_b32_sdwa v23, v18, v177 dst_sel:DWORD dst_unused:UNUSED_PAD src0_sel:WORD_1 src1_sel:DWORD
	v_exp_f32_e32 v22, v22
	v_add3_u32 v18, v18, v23, s63
	v_and_b32_e32 v18, 0xffff0000, v18
	v_or_b32_sdwa v18, v18, v21 dst_sel:DWORD dst_unused:UNUSED_PAD src0_sel:DWORD src1_sel:WORD_1
	global_store_dwordx2 v[74:75], v[18:19], off offset:352
	v_lshlrev_b32_e32 v21, 16, v245
	v_add_f32_e32 v18, 1.0, v22
	v_and_b32_e32 v22, 0xffff0000, v244
	v_mul_f32_e32 v19, 0xbfb8aa3b, v22
	v_mul_f32_e32 v24, 0xbfb8aa3b, v21
	v_exp_f32_e32 v19, v19
	v_exp_f32_e32 v25, v24
	v_and_b32_e32 v23, 0xffff0000, v245
	v_rcp_f32_e32 v18, v18
	v_add_f32_e32 v19, 1.0, v19
	v_add_f32_e32 v14, 1.0, v25
	v_rcp_f32_e32 v24, v19
	v_rcp_f32_e32 v19, v14
	v_mul_f32_e32 v14, 0xbfb8aa3b, v23
	v_exp_f32_e32 v14, v14
	v_mov_b32_e32 v27, v16
	v_pk_mul_f32 v[26:27], v[26:27], v[66:67] op_sel_hi:[1,0]
	v_pk_mul_f32 v[18:19], v[18:19], v[20:21]
	v_add_f32_e32 v14, 1.0, v14
	v_rcp_f32_e32 v25, v14
	v_mov_b32_e32 v16, v15
	v_pk_mul_f32 v[18:19], v[26:27], v[18:19]
	v_pk_mul_f32 v[14:15], v[16:17], v[66:67] op_sel_hi:[1,0]
	v_pk_mul_f32 v[16:17], v[24:25], v[22:23]
	v_mov_b32_e32 v22, v10
	v_pk_mul_f32 v[14:15], v[14:15], v[16:17]
	v_and_b32_sdwa v17, v18, v177 dst_sel:DWORD dst_unused:UNUSED_PAD src0_sel:WORD_1 src1_sel:DWORD
	v_add3_u32 v17, v18, v17, s63
	v_and_b32_sdwa v18, v15, v177 dst_sel:DWORD dst_unused:UNUSED_PAD src0_sel:WORD_1 src1_sel:DWORD
	v_and_b32_sdwa v16, v19, v177 dst_sel:DWORD dst_unused:UNUSED_PAD src0_sel:WORD_1 src1_sel:DWORD
	v_add3_u32 v15, v15, v18, s63
	v_add3_u32 v16, v19, v16, s63
	v_and_b32_e32 v15, 0xffff0000, v15
	v_or_b32_sdwa v15, v15, v16 dst_sel:DWORD dst_unused:UNUSED_PAD src0_sel:DWORD src1_sel:WORD_1
	v_lshlrev_b32_e32 v16, 16, v76
	v_mul_f32_e32 v18, 0xbfb8aa3b, v16
	v_and_b32_sdwa v19, v14, v177 dst_sel:DWORD dst_unused:UNUSED_PAD src0_sel:WORD_1 src1_sel:DWORD
	v_exp_f32_e32 v18, v18
	v_add3_u32 v14, v14, v19, s63
	v_and_b32_e32 v14, 0xffff0000, v14
	v_or_b32_sdwa v14, v14, v17 dst_sel:DWORD dst_unused:UNUSED_PAD src0_sel:DWORD src1_sel:WORD_1
	global_store_dwordx2 v[74:75], v[14:15], off offset:384
	v_lshlrev_b32_e32 v17, 16, v77
	v_add_f32_e32 v14, 1.0, v18
	v_and_b32_e32 v18, 0xffff0000, v76
	v_mul_f32_e32 v15, 0xbfb8aa3b, v18
	v_mul_f32_e32 v20, 0xbfb8aa3b, v17
	v_exp_f32_e32 v15, v15
	v_exp_f32_e32 v21, v20
	v_and_b32_e32 v19, 0xffff0000, v77
	v_rcp_f32_e32 v14, v14
	v_add_f32_e32 v15, 1.0, v15
	v_add_f32_e32 v10, 1.0, v21
	v_rcp_f32_e32 v20, v15
	v_rcp_f32_e32 v15, v10
	v_mul_f32_e32 v10, 0xbfb8aa3b, v19
	v_exp_f32_e32 v10, v10
	v_mov_b32_e32 v23, v12
	v_pk_mul_f32 v[22:23], v[22:23], v[66:67] op_sel_hi:[1,0]
	v_pk_mul_f32 v[14:15], v[14:15], v[16:17]
	v_add_f32_e32 v10, 1.0, v10
	v_rcp_f32_e32 v21, v10
	v_mov_b32_e32 v12, v11
	v_pk_mul_f32 v[14:15], v[22:23], v[14:15]
	v_pk_mul_f32 v[10:11], v[12:13], v[66:67] op_sel_hi:[1,0]
	v_pk_mul_f32 v[12:13], v[20:21], v[18:19]
	v_mov_b32_e32 v18, v6
	v_pk_mul_f32 v[10:11], v[10:11], v[12:13]
	v_and_b32_sdwa v13, v14, v177 dst_sel:DWORD dst_unused:UNUSED_PAD src0_sel:WORD_1 src1_sel:DWORD
	v_add3_u32 v13, v14, v13, s63
	v_and_b32_sdwa v14, v11, v177 dst_sel:DWORD dst_unused:UNUSED_PAD src0_sel:WORD_1 src1_sel:DWORD
	v_and_b32_sdwa v12, v15, v177 dst_sel:DWORD dst_unused:UNUSED_PAD src0_sel:WORD_1 src1_sel:DWORD
	v_add3_u32 v11, v11, v14, s63
	v_add3_u32 v12, v15, v12, s63
	v_and_b32_e32 v11, 0xffff0000, v11
	v_or_b32_sdwa v11, v11, v12 dst_sel:DWORD dst_unused:UNUSED_PAD src0_sel:DWORD src1_sel:WORD_1
	v_lshlrev_b32_e32 v12, 16, v78
	v_mul_f32_e32 v14, 0xbfb8aa3b, v12
	v_and_b32_sdwa v15, v10, v177 dst_sel:DWORD dst_unused:UNUSED_PAD src0_sel:WORD_1 src1_sel:DWORD
	v_exp_f32_e32 v14, v14
	v_add3_u32 v10, v10, v15, s63
	v_and_b32_e32 v10, 0xffff0000, v10
	v_or_b32_sdwa v10, v10, v13 dst_sel:DWORD dst_unused:UNUSED_PAD src0_sel:DWORD src1_sel:WORD_1
	global_store_dwordx2 v[74:75], v[10:11], off offset:416
	v_lshlrev_b32_e32 v13, 16, v79
	v_add_f32_e32 v10, 1.0, v14
	v_and_b32_e32 v14, 0xffff0000, v78
	v_mul_f32_e32 v11, 0xbfb8aa3b, v14
	v_mul_f32_e32 v16, 0xbfb8aa3b, v13
	v_exp_f32_e32 v11, v11
	v_exp_f32_e32 v17, v16
	v_and_b32_e32 v15, 0xffff0000, v79
	v_rcp_f32_e32 v10, v10
	v_add_f32_e32 v11, 1.0, v11
	v_add_f32_e32 v6, 1.0, v17
	v_rcp_f32_e32 v16, v11
	v_rcp_f32_e32 v11, v6
	v_mul_f32_e32 v6, 0xbfb8aa3b, v15
	v_exp_f32_e32 v6, v6
	v_mov_b32_e32 v19, v8
	v_pk_mul_f32 v[18:19], v[18:19], v[66:67] op_sel_hi:[1,0]
	v_pk_mul_f32 v[10:11], v[10:11], v[12:13]
	v_add_f32_e32 v6, 1.0, v6
	v_rcp_f32_e32 v17, v6
	v_mov_b32_e32 v8, v7
	v_pk_mul_f32 v[10:11], v[18:19], v[10:11]
	v_pk_mul_f32 v[6:7], v[8:9], v[66:67] op_sel_hi:[1,0]
	v_pk_mul_f32 v[8:9], v[16:17], v[14:15]
	v_mov_b32_e32 v14, v2
	v_pk_mul_f32 v[6:7], v[6:7], v[8:9]
	v_and_b32_sdwa v9, v10, v177 dst_sel:DWORD dst_unused:UNUSED_PAD src0_sel:WORD_1 src1_sel:DWORD
	v_add3_u32 v9, v10, v9, s63
	v_and_b32_sdwa v10, v7, v177 dst_sel:DWORD dst_unused:UNUSED_PAD src0_sel:WORD_1 src1_sel:DWORD
	v_and_b32_sdwa v8, v11, v177 dst_sel:DWORD dst_unused:UNUSED_PAD src0_sel:WORD_1 src1_sel:DWORD
	v_add3_u32 v7, v7, v10, s63
	v_add3_u32 v8, v11, v8, s63
	v_and_b32_e32 v7, 0xffff0000, v7
	v_or_b32_sdwa v7, v7, v8 dst_sel:DWORD dst_unused:UNUSED_PAD src0_sel:DWORD src1_sel:WORD_1
	v_lshlrev_b32_e32 v8, 16, v80
	v_mul_f32_e32 v10, 0xbfb8aa3b, v8
	v_and_b32_sdwa v11, v6, v177 dst_sel:DWORD dst_unused:UNUSED_PAD src0_sel:WORD_1 src1_sel:DWORD
	v_exp_f32_e32 v10, v10
	v_add3_u32 v6, v6, v11, s63
	v_and_b32_e32 v6, 0xffff0000, v6
	v_or_b32_sdwa v6, v6, v9 dst_sel:DWORD dst_unused:UNUSED_PAD src0_sel:DWORD src1_sel:WORD_1
	global_store_dwordx2 v[74:75], v[6:7], off offset:448
	v_lshlrev_b32_e32 v9, 16, v81
	v_add_f32_e32 v6, 1.0, v10
	v_and_b32_e32 v10, 0xffff0000, v80
	v_mul_f32_e32 v7, 0xbfb8aa3b, v10
	v_mul_f32_e32 v12, 0xbfb8aa3b, v9
	v_exp_f32_e32 v7, v7
	v_exp_f32_e32 v13, v12
	v_and_b32_e32 v11, 0xffff0000, v81
	v_rcp_f32_e32 v6, v6
	v_add_f32_e32 v7, 1.0, v7
	v_add_f32_e32 v2, 1.0, v13
	v_rcp_f32_e32 v12, v7
	v_rcp_f32_e32 v7, v2
	v_mul_f32_e32 v2, 0xbfb8aa3b, v11
	v_exp_f32_e32 v2, v2
	v_mov_b32_e32 v15, v4
	v_pk_mul_f32 v[14:15], v[14:15], v[66:67] op_sel_hi:[1,0]
	v_pk_mul_f32 v[6:7], v[6:7], v[8:9]
	v_add_f32_e32 v2, 1.0, v2
	v_rcp_f32_e32 v13, v2
	v_mov_b32_e32 v4, v3
	v_pk_mul_f32 v[6:7], v[14:15], v[6:7]
	v_pk_mul_f32 v[2:3], v[4:5], v[66:67] op_sel_hi:[1,0]
	v_pk_mul_f32 v[4:5], v[12:13], v[10:11]
	s_nop 0
	v_pk_mul_f32 v[2:3], v[2:3], v[4:5]
	v_and_b32_sdwa v4, v7, v177 dst_sel:DWORD dst_unused:UNUSED_PAD src0_sel:WORD_1 src1_sel:DWORD
	v_and_b32_sdwa v5, v6, v177 dst_sel:DWORD dst_unused:UNUSED_PAD src0_sel:WORD_1 src1_sel:DWORD
	v_add3_u32 v5, v6, v5, s63
	v_add3_u32 v4, v7, v4, s63
	v_and_b32_sdwa v6, v3, v177 dst_sel:DWORD dst_unused:UNUSED_PAD src0_sel:WORD_1 src1_sel:DWORD
	v_and_b32_sdwa v7, v2, v177 dst_sel:DWORD dst_unused:UNUSED_PAD src0_sel:WORD_1 src1_sel:DWORD
	v_add3_u32 v3, v3, v6, s63
	v_add3_u32 v2, v2, v7, s63
	v_and_b32_e32 v3, 0xffff0000, v3
	v_and_b32_e32 v2, 0xffff0000, v2
	v_or_b32_sdwa v3, v3, v4 dst_sel:DWORD dst_unused:UNUSED_PAD src0_sel:DWORD src1_sel:WORD_1
	v_or_b32_sdwa v2, v2, v5 dst_sel:DWORD dst_unused:UNUSED_PAD src0_sel:DWORD src1_sel:WORD_1
	global_store_dwordx2 v[74:75], v[2:3], off offset:480
	s_cbranch_scc1 .LBB0_389

.LBB0_979:
	s_ashr_i32 s19, s16, 31
	s_lshr_b32 s19, s19, 21
	s_add_i32 s16, s16, s19
	s_ashr_i32 s19, s18, 31
	s_ashr_i32 s21, s20, 31
	s_lshl_b64 s[18:19], s[18:19], 12
	s_ashr_i32 s16, s16, 11
	v_lshl_add_u64 v[44:45], v[38:39], 0, s[18:19]
	s_lshl_b64 s[18:19], s[20:21], 12
	v_lshl_add_u64 v[46:47], v[38:39], 0, s[18:19]
	s_mul_hi_i32 s19, s16, 0xc000
	s_mul_i32 s16, s16, 0xc000
	global_load_dwordx2 v[56:57], v[46:47], off
	global_load_dwordx2 v[58:59], v[44:45], off
	s_add_u32 s18, s10, s16
	global_load_dwordx2 v[104:105], v[46:47], off offset:512
	global_load_dwordx2 v[106:107], v[44:45], off offset:512
	s_addc_u32 s19, s11, s19
	v_lshl_add_u64 v[48:49], s[18:19], 0, v[32:33]
	v_lshl_add_u64 v[108:109], v[48:49], 0, s[2:3]
	v_add_co_u32_e32 v48, vcc, s31, v48
	v_lshl_add_u64 v[50:51], s[12:13], 0, v[34:35]
	s_nop 0
	v_addc_co_u32_e32 v49, vcc, 0, v49, vcc
	global_load_dwordx4 v[52:55], v[48:49], off offset:-4096
	global_load_dwordx2 v[110:111], v[46:47], off offset:1024
	global_load_dwordx2 v[112:113], v[44:45], off offset:1024
	v_add_co_u32_e32 v114, vcc, s29, v50
	s_mov_b32 s16, s36
	s_nop 0
	v_addc_co_u32_e32 v115, vcc, 0, v51, vcc
	v_add_co_u32_e32 v50, vcc, s33, v50
	s_waitcnt vmcnt(6)
	v_lshlrev_b32_e32 v128, 16, v57
	v_addc_co_u32_e32 v51, vcc, 0, v51, vcc
	global_load_dwordx4 v[68:71], v[50:51], off offset:-4096
	global_load_dwordx4 v[72:75], v[108:109], off offset:1024
	global_load_dwordx4 v[76:79], v[114:115], off offset:1024
	global_load_dwordx4 v[80:83], v[114:115], off offset:2048
	global_load_dwordx4 v[84:87], v[108:109], off offset:2048
	global_load_dwordx2 v[116:117], v[46:47], off offset:1536
	global_load_dwordx2 v[118:119], v[44:45], off offset:1536
	global_load_dwordx4 v[88:91], v[114:115], off offset:3072
	global_load_dwordx4 v[92:95], v[50:51], off
	global_load_dwordx2 v[120:121], v[44:45], off offset:2048
	global_load_dwordx2 v[122:123], v[44:45], off offset:2560
	global_load_dwordx2 v[124:125], v[46:47], off offset:2048
	global_load_dwordx2 v[126:127], v[46:47], off offset:2560
	global_load_dwordx4 v[96:99], v[108:109], off offset:3072
	global_load_dwordx4 v[100:103], v[48:49], off
	v_lshlrev_b32_e32 v108, 16, v56
	s_waitcnt vmcnt(20)
	v_and_b32_e32 v109, 0xffff0000, v58
	v_lshlrev_b32_e32 v114, 16, v58
	v_and_b32_e32 v115, 0xffff0000, v56
	v_lshlrev_b32_e32 v56, 16, v59
	v_and_b32_e32 v57, 0xffff0000, v57
	s_waitcnt vmcnt(19)
	v_lshlrev_b32_e32 v58, 16, v104
	s_waitcnt vmcnt(18)
	v_lshlrev_b32_e32 v130, 16, v106
	v_and_b32_e32 v131, 0xffff0000, v104
	v_lshlrev_b32_e32 v132, 16, v105
	v_lshlrev_b32_e32 v104, 16, v107
	v_and_b32_e32 v105, 0xffff0000, v105
	v_and_b32_e32 v129, 0xffff0000, v59
	v_and_b32_e32 v59, 0xffff0000, v106
	v_and_b32_e32 v133, 0xffff0000, v107
	v_pk_mul_f32 v[114:115], v[42:43], v[114:115]
	v_pk_mul_f32 v[56:57], v[42:43], v[56:57]
	v_pk_mul_f32 v[130:131], v[42:43], v[130:131]
	v_pk_mul_f32 v[104:105], v[42:43], v[104:105]
	v_pk_fma_f32 v[108:109], v[42:43], v[108:109], v[114:115] op_sel:[1,0,0] op_sel_hi:[0,1,1]
	v_pk_fma_f32 v[56:57], v[42:43], v[128:129], v[56:57] op_sel:[1,0,0] op_sel_hi:[0,1,1]
	v_pk_fma_f32 v[114:115], v[42:43], v[58:59], v[130:131] op_sel:[1,0,0] op_sel_hi:[0,1,1]
	v_pk_fma_f32 v[104:105], v[42:43], v[132:133], v[104:105] op_sel:[1,0,0] op_sel_hi:[0,1,1]
	s_waitcnt vmcnt(16)
	v_lshlrev_b32_e32 v106, 16, v110
	s_waitcnt vmcnt(15)
	v_and_b32_e32 v107, 0xffff0000, v112
	s_waitcnt vmcnt(14)
	v_pk_fma_f32 v[56:57], v[54:55], v[56:57], v[70:71]
	v_pk_fma_f32 v[58:59], v[52:53], v[108:109], v[68:69]
	s_waitcnt vmcnt(12)
	v_pk_fma_f32 v[52:53], v[74:75], v[104:105], v[78:79]
	v_pk_fma_f32 v[54:55], v[72:73], v[114:115], v[76:77]
	v_mov_b32_e32 v70, v59
	v_mov_b32_e32 v71, v55
	v_mov_b32_e32 v74, v57
	v_mov_b32_e32 v75, v53
	v_mov_b32_e32 v68, v58
	v_mov_b32_e32 v69, v54
	v_mov_b32_e32 v72, v56
	v_mov_b32_e32 v73, v52
	v_pk_mul_f32 v[70:71], v[70:71], v[70:71]
	v_pk_mul_f32 v[74:75], v[74:75], v[74:75]
	v_pk_fma_f32 v[68:69], v[68:69], v[68:69], v[70:71]
	v_pk_fma_f32 v[70:71], v[72:73], v[72:73], v[74:75]
	v_lshlrev_b32_e32 v78, 16, v111
	v_pk_add_f32 v[104:105], v[68:69], v[70:71]
	v_lshlrev_b32_e32 v68, 16, v112
	v_and_b32_e32 v69, 0xffff0000, v110
	v_pk_mul_f32 v[76:77], v[42:43], v[68:69]
	global_load_dwordx4 v[68:71], v[48:49], off offset:1024
	global_load_dwordx4 v[72:75], v[50:51], off offset:1024
	v_pk_fma_f32 v[76:77], v[42:43], v[106:107], v[76:77] op_sel:[1,0,0] op_sel_hi:[0,1,1]
	v_lshlrev_b32_e32 v106, 16, v113
	v_and_b32_e32 v107, 0xffff0000, v111
	v_and_b32_e32 v79, 0xffff0000, v113
	v_pk_mul_f32 v[106:107], v[42:43], v[106:107]
	global_load_dwordx2 v[108:109], v[46:47], off offset:3072
	global_load_dwordx2 v[110:111], v[44:45], off offset:3072
	v_pk_fma_f32 v[78:79], v[42:43], v[78:79], v[106:107] op_sel:[1,0,0] op_sel_hi:[0,1,1]
	s_waitcnt vmcnt(14)
	v_pk_fma_f32 v[84:85], v[84:85], v[76:77], v[80:81]
	v_pk_fma_f32 v[86:87], v[86:87], v[78:79], v[82:83]
	v_pk_mul_f32 v[78:79], v[84:85], v[84:85]
	v_pk_mul_f32 v[76:77], v[86:87], v[86:87]
	s_waitcnt vmcnt(13)
	v_lshlrev_b32_e32 v112, 16, v116
	v_pk_mov_b32 v[80:81], v[78:79], v[76:77] op_sel:[1,0]
	v_mov_b32_e32 v79, v77
	v_pk_add_f32 v[106:107], v[80:81], v[78:79]
	global_load_dwordx4 v[76:79], v[48:49], off offset:2048
	global_load_dwordx4 v[80:83], v[50:51], off offset:2048
	global_load_dwordx2 v[114:115], v[46:47], off offset:3584
	global_load_dwordx2 v[128:129], v[44:45], off offset:3584
	s_waitcnt vmcnt(16)
	v_lshlrev_b32_e32 v44, 16, v118
	v_and_b32_e32 v45, 0xffff0000, v116
	v_and_b32_e32 v113, 0xffff0000, v118
	v_pk_mul_f32 v[44:45], v[42:43], v[44:45]
	v_lshlrev_b32_e32 v130, 16, v117
	v_pk_fma_f32 v[112:113], v[42:43], v[112:113], v[44:45] op_sel:[1,0,0] op_sel_hi:[0,1,1]
	v_lshlrev_b32_e32 v44, 16, v119
	v_and_b32_e32 v45, 0xffff0000, v117
	v_pk_mul_f32 v[116:117], v[42:43], v[44:45]
	global_load_dwordx4 v[44:47], v[48:49], off offset:3072
	s_nop 0
	global_load_dwordx4 v[48:51], v[50:51], off offset:3072
	v_and_b32_e32 v131, 0xffff0000, v119
	v_pk_fma_f32 v[116:117], v[42:43], v[130:131], v[116:117] op_sel:[1,0,0] op_sel_hi:[0,1,1]
	s_waitcnt vmcnt(11)
	v_pk_fma_f32 v[90:91], v[98:99], v[116:117], v[90:91]
	v_lshlrev_b32_e32 v98, 16, v120
	v_and_b32_e32 v99, 0xffff0000, v124
	v_pk_fma_f32 v[88:89], v[96:97], v[112:113], v[88:89]
	v_lshlrev_b32_e32 v96, 16, v124
	v_and_b32_e32 v97, 0xffff0000, v120
	v_pk_mul_f32 v[98:99], v[42:43], v[98:99]
	v_lshlrev_b32_e32 v112, 16, v121
	v_and_b32_e32 v113, 0xffff0000, v125
	v_pk_fma_f32 v[96:97], v[42:43], v[96:97], v[98:99] op_sel:[1,0,0] op_sel_hi:[0,1,1]
	v_lshlrev_b32_e32 v98, 16, v125
	v_and_b32_e32 v99, 0xffff0000, v121
	v_pk_mul_f32 v[112:113], v[42:43], v[112:113]
	s_waitcnt vmcnt(10)
	v_pk_fma_f32 v[92:93], v[100:101], v[96:97], v[92:93]
	v_pk_fma_f32 v[98:99], v[42:43], v[98:99], v[112:113] op_sel:[1,0,0] op_sel_hi:[0,1,1]
	v_pk_fma_f32 v[94:95], v[102:103], v[98:99], v[94:95]
	v_mul_f32_e32 v67, v92, v92
	v_mul_f32_e32 v100, v93, v93
	v_pk_add_f32 v[96:97], v[104:105], v[104:105] op_sel:[0,1] op_sel_hi:[1,0]
	v_pk_add_f32 v[98:99], v[106:107], v[106:107] op_sel:[0,1] op_sel_hi:[1,0]
	v_mov_b32_e32 v97, v67
	v_mov_b32_e32 v99, v100
	v_pk_add_f32 v[96:97], v[96:97], v[98:99]
	v_mul_f32_e32 v98, v89, v89
	v_mul_f32_e32 v101, v94, v94
	v_pk_fma_f32 v[98:99], v[88:89], v[88:89], v[98:99] op_sel_hi:[1,1,0]
	v_mul_f32_e32 v100, v91, v91
	v_mul_f32_e32 v102, v95, v95
	v_mov_b32_e32 v99, v101
	v_pk_fma_f32 v[100:101], v[90:91], v[90:91], v[100:101] op_sel_hi:[1,1,0]
	v_and_b32_e32 v103, 0xffff0000, v127
	v_mov_b32_e32 v101, v102
	v_pk_add_f32 v[98:99], v[98:99], v[100:101]
	v_lshlrev_b32_e32 v100, 16, v122
	v_and_b32_e32 v101, 0xffff0000, v126
	v_pk_add_f32 v[96:97], v[96:97], v[98:99]
	v_lshlrev_b32_e32 v98, 16, v126
	v_and_b32_e32 v99, 0xffff0000, v122
	v_pk_mul_f32 v[100:101], v[42:43], v[100:101]
	v_lshlrev_b32_e32 v102, 16, v123
	v_pk_fma_f32 v[98:99], v[42:43], v[98:99], v[100:101] op_sel:[1,0,0] op_sel_hi:[0,1,1]
	v_lshlrev_b32_e32 v100, 16, v127
	v_and_b32_e32 v101, 0xffff0000, v123
	v_pk_mul_f32 v[102:103], v[42:43], v[102:103]
	s_waitcnt vmcnt(8)
	v_pk_fma_f32 v[68:69], v[68:69], v[98:99], v[72:73]
	v_pk_fma_f32 v[100:101], v[42:43], v[100:101], v[102:103] op_sel:[1,0,0] op_sel_hi:[0,1,1]
	v_pk_fma_f32 v[70:71], v[70:71], v[100:101], v[74:75]
	v_pk_mul_f32 v[74:75], v[68:69], v[68:69]
	v_pk_mul_f32 v[72:73], v[70:71], v[70:71]
	s_waitcnt vmcnt(7)
	v_and_b32_e32 v101, 0xffff0000, v109
	v_pk_mov_b32 v[98:99], v[74:75], v[72:73] op_sel:[1,0]
	v_mov_b32_e32 v75, v73
	v_pk_add_f32 v[72:73], v[98:99], v[74:75]
	s_waitcnt vmcnt(6)
	v_lshlrev_b32_e32 v98, 16, v110
	v_and_b32_e32 v99, 0xffff0000, v108
	v_lshlrev_b32_e32 v74, 16, v108
	v_and_b32_e32 v75, 0xffff0000, v110
	v_pk_mul_f32 v[98:99], v[42:43], v[98:99]
	v_lshlrev_b32_e32 v100, 16, v111
	v_pk_fma_f32 v[74:75], v[42:43], v[74:75], v[98:99] op_sel:[1,0,0] op_sel_hi:[0,1,1]
	v_lshlrev_b32_e32 v98, 16, v109
	v_and_b32_e32 v99, 0xffff0000, v111
	v_pk_mul_f32 v[100:101], v[42:43], v[100:101]
	s_waitcnt vmcnt(4)
	v_pk_fma_f32 v[74:75], v[76:77], v[74:75], v[80:81]
	v_pk_fma_f32 v[98:99], v[42:43], v[98:99], v[100:101] op_sel:[1,0,0] op_sel_hi:[0,1,1]
	s_waitcnt vmcnt(2)
	v_lshlrev_b32_e32 v80, 16, v128
	v_and_b32_e32 v81, 0xffff0000, v114
	v_pk_fma_f32 v[78:79], v[78:79], v[98:99], v[82:83]
	v_lshlrev_b32_e32 v76, 16, v114
	v_and_b32_e32 v77, 0xffff0000, v128
	v_pk_mul_f32 v[80:81], v[42:43], v[80:81]
	v_lshlrev_b32_e32 v82, 16, v129
	v_and_b32_e32 v83, 0xffff0000, v115
	v_pk_fma_f32 v[76:77], v[42:43], v[76:77], v[80:81] op_sel:[1,0,0] op_sel_hi:[0,1,1]
	v_lshlrev_b32_e32 v80, 16, v115
	v_and_b32_e32 v81, 0xffff0000, v129
	v_pk_mul_f32 v[82:83], v[42:43], v[82:83]
	s_waitcnt vmcnt(0)
	v_pk_fma_f32 v[48:49], v[44:45], v[76:77], v[48:49]
	v_pk_fma_f32 v[42:43], v[42:43], v[80:81], v[82:83] op_sel:[1,0,0] op_sel_hi:[0,1,1]
	v_pk_fma_f32 v[46:47], v[46:47], v[42:43], v[50:51]
	v_mul_f32_e32 v44, v48, v48
	v_pk_add_f32 v[42:43], v[96:97], v[96:97] op_sel:[0,1] op_sel_hi:[1,0]
	v_mul_f32_e32 v50, v49, v49
	v_mov_b32_e32 v43, v44
	v_pk_add_f32 v[44:45], v[72:73], v[72:73] op_sel:[0,1] op_sel_hi:[1,0]
	v_mul_f32_e32 v51, v46, v46
	v_mov_b32_e32 v45, v50
	v_pk_add_f32 v[42:43], v[42:43], v[44:45]
	v_mul_f32_e32 v44, v75, v75
	v_pk_fma_f32 v[44:45], v[74:75], v[74:75], v[44:45] op_sel_hi:[1,1,0]
	v_mul_f32_e32 v50, v79, v79
	v_mul_f32_e32 v67, v47, v47
	v_mov_b32_e32 v45, v51
	v_pk_fma_f32 v[50:51], v[78:79], v[78:79], v[50:51] op_sel_hi:[1,1,0]
	v_lshl_add_u64 v[72:73], s[4:5], 0, v[34:35]
	v_mov_b32_e32 v51, v67
	v_pk_add_f32 v[44:45], v[44:45], v[50:51]
	s_add_u32 s4, s4, s6
	v_pk_add_f32 v[42:43], v[42:43], v[44:45]
	s_addc_u32 s5, s5, s7
	v_add_f32_e32 v42, v42, v43
	ds_bpermute_b32 v43, v60, v42
	s_add_i32 s8, s8, s17
	s_add_u32 s12, s12, s6
	s_addc_u32 s13, s13, s7
	s_waitcnt lgkmcnt(0)
	v_add_f32_e32 v42, v42, v43
	ds_bpermute_b32 v43, v61, v42
	s_waitcnt lgkmcnt(0)
	v_add_f32_e32 v42, v42, v43
	ds_bpermute_b32 v43, v62, v42
	s_waitcnt lgkmcnt(0)
	v_add_f32_e32 v42, v42, v43
	ds_bpermute_b32 v43, v63, v42
	s_waitcnt lgkmcnt(0)
	v_add_f32_e32 v42, v42, v43
	ds_bpermute_b32 v43, v64, v42
	s_waitcnt lgkmcnt(0)
	v_add_f32_e32 v42, v42, v43
	ds_bpermute_b32 v43, v65, v42
	s_waitcnt lgkmcnt(0)
	v_add_f32_e32 v42, v42, v43
	v_fmamk_f32 v42, v42, 0x3a000000, v66
	v_mul_f32_e32 v43, 0x4b800000, v42
	v_cmp_gt_f32_e32 vcc, s34, v42
	s_nop 1
	v_cndmask_b32_e32 v42, v42, v43, vcc
	v_rsq_f32_e32 v42, v42
	s_nop 0
	v_mul_f32_e32 v43, 0x45800000, v42
	v_cndmask_b32_e32 v50, v42, v43, vcc
	v_pk_mul_f32 v[42:43], v[58:59], v[50:51] op_sel_hi:[1,0]
	v_pk_mul_f32 v[44:45], v[56:57], v[50:51] op_sel_hi:[1,0]
	v_pk_mul_f32 v[42:43], v[0:1], v[42:43]
	v_pk_mul_f32 v[44:45], v[2:3], v[44:45]
	global_store_dwordx4 v[72:73], v[42:45], off
	s_nop 1
	v_pk_mul_f32 v[42:43], v[54:55], v[50:51] op_sel_hi:[1,0]
	v_pk_mul_f32 v[44:45], v[52:53], v[50:51] op_sel_hi:[1,0]
	v_pk_mul_f32 v[42:43], v[4:5], v[42:43]
	v_pk_mul_f32 v[44:45], v[6:7], v[44:45]
	global_store_dwordx4 v[72:73], v[42:45], off offset:1024
	v_add_co_u32_e32 v52, vcc, s28, v72
	s_nop 0
	v_pk_mul_f32 v[42:43], v[84:85], v[50:51] op_sel_hi:[1,0]
	v_pk_mul_f32 v[44:45], v[86:87], v[50:51] op_sel_hi:[1,0]
	v_pk_mul_f32 v[42:43], v[8:9], v[42:43]
	v_pk_mul_f32 v[44:45], v[10:11], v[44:45]
	global_store_dwordx4 v[72:73], v[42:45], off offset:2048
	v_addc_co_u32_e32 v53, vcc, 0, v73, vcc
	s_nop 0
	v_pk_mul_f32 v[42:43], v[88:89], v[50:51] op_sel_hi:[1,0]
	v_pk_mul_f32 v[44:45], v[90:91], v[50:51] op_sel_hi:[1,0]
	v_pk_mul_f32 v[42:43], v[12:13], v[42:43]
	v_pk_mul_f32 v[44:45], v[14:15], v[44:45]
	global_store_dwordx4 v[72:73], v[42:45], off offset:3072
	s_andn2_b64 vcc, exec, s[14:15]
	s_nop 0
	v_pk_mul_f32 v[42:43], v[92:93], v[50:51] op_sel_hi:[1,0]
	v_pk_mul_f32 v[44:45], v[94:95], v[50:51] op_sel_hi:[1,0]
	v_pk_mul_f32 v[42:43], v[16:17], v[42:43]
	v_pk_mul_f32 v[44:45], v[18:19], v[44:45]
	global_store_dwordx4 v[52:53], v[42:45], off
	s_nop 1
	v_pk_mul_f32 v[42:43], v[68:69], v[50:51] op_sel_hi:[1,0]
	v_pk_mul_f32 v[44:45], v[70:71], v[50:51] op_sel_hi:[1,0]
	v_pk_mul_f32 v[42:43], v[20:21], v[42:43]
	v_pk_mul_f32 v[44:45], v[22:23], v[44:45]
	global_store_dwordx4 v[52:53], v[42:45], off offset:1024
	s_nop 1
	v_pk_mul_f32 v[42:43], v[74:75], v[50:51] op_sel_hi:[1,0]
	v_pk_mul_f32 v[44:45], v[78:79], v[50:51] op_sel_hi:[1,0]
	v_pk_mul_f32 v[42:43], v[24:25], v[42:43]
	v_pk_mul_f32 v[44:45], v[26:27], v[44:45]
	global_store_dwordx4 v[52:53], v[42:45], off offset:2048
	s_nop 1
	v_pk_mul_f32 v[42:43], v[48:49], v[50:51] op_sel_hi:[1,0]
	v_pk_mul_f32 v[44:45], v[46:47], v[50:51] op_sel_hi:[1,0]
	v_pk_mul_f32 v[42:43], v[28:29], v[42:43]
	v_pk_mul_f32 v[44:45], v[30:31], v[44:45]
	global_store_dwordx4 v[52:53], v[42:45], off offset:3072
	s_nop 1
	v_mov_b64_e32 v[42:43], v[40:41]
	v_readfirstlane_b32 s9, v200
	v_readfirstlane_b32 s35, v201
	s_nop 3
	s_cbranch_vccz .LBB0_982
.LBB0_980:
	s_ashr_i32 s14, s9, 31
	s_lshr_b32 s14, s14, 23
	s_add_i32 s14, s9, s14
	s_ashr_i32 s15, s14, 9
	v_lshlrev_b32_e32 v45, 6, v36
	v_add_u32_e32 v45, s30, v45
	s_lshl_b32 s15, s15, 2
	v_add_u32_e32 v45, s15, v45
	s_ashr_i32 s15, s35, 31
	s_lshr_b32 s15, s15, 23
	v_lshlrev_b32_e32 v44, 2, v36
	s_add_i32 s15, s35, s15
	v_add_u32_e32 v44, s1, v44
	s_ashr_i32 s18, s15, 9
	v_lshlrev_b32_e32 v47, 6, v37
	ds_read_b32 v44, v44
	v_lshlrev_b32_e32 v46, 2, v37
	v_add_u32_e32 v47, s30, v47
	s_lshl_b32 s18, s18, 2
	v_add_u32_e32 v46, s1, v46
	v_add_u32_e32 v47, s18, v47
	ds_read_b32 v45, v45
	ds_read_b32 v47, v47
	ds_read_b32 v46, v46
	s_and_b32 s14, s14, 0xfffffe00
	s_sub_i32 s14, s9, s14
	s_waitcnt lgkmcnt(3)
	v_lshlrev_b32_e32 v44, 8, v44
	s_waitcnt lgkmcnt(2)
	v_add_u32_e32 v45, s14, v45
	s_and_b32 s14, s15, 0xfffffe00
	v_add_u32_e32 v44, v45, v44
	s_sub_i32 s14, s35, s14
	s_add_i32 s36, s16, s0
	v_readfirstlane_b32 s18, v44
	s_waitcnt lgkmcnt(0)
	v_lshlrev_b32_e32 v44, 8, v46
	v_add_u32_e32 v45, s14, v47
	s_cmpk_gt_i32 s36, 0x1fff
	v_add_u32_e32 v44, v45, v44
	s_cselect_b64 s[14:15], -1, 0
	v_readfirstlane_b32 s20, v44
	s_and_b64 vcc, exec, s[14:15]
	s_cbranch_vccnz .LBB0_979
	s_ashr_i32 s9, s8, 31
	s_lshl_b64 s[38:39], s[8:9], 2
	s_add_u32 s40, s22, s38
	s_addc_u32 s41, s23, s39
	s_add_i32 s42, s8, 1
	s_ashr_i32 s43, s42, 31
	s_add_u32 s44, s24, s38
	s_addc_u32 s45, s25, s39
	s_lshl_b64 s[42:43], s[42:43], 2
	s_add_u32 s46, s24, s42
	s_addc_u32 s47, s25, s43
	s_add_u32 s38, s26, s38
	s_addc_u32 s39, s27, s39
	s_add_u32 s42, s26, s42
	s_addc_u32 s43, s27, s43
	global_load_dwordx2 v[36:37], v33, s[40:41]
	global_load_dword v200, v33, s[44:45]
	global_load_dword v201, v33, s[46:47]
	global_load_dword v40, v33, s[38:39]
	global_load_dword v41, v33, s[42:43]
	s_branch .LBB0_979
